# mod_items preamble: the 20 silu input loads per thread issued together (was a 20-step load-wait loop), same IEEE-division sequence
# baseline (speedup 1.0000x reference)
; #define LAS __attribute__((address_space(3)))
; __device__ __forceinline__ float sigmoid_(float x) { return 1.f / (1.f + __expf(-x)); }
; __device__ __forceinline__ float silu_(float x) { return x * sigmoid_(x); }
; __device__ __forceinline__ void mod_items(const Args& a, const Ctx& c0, int l) {
;     ...
;     LAS float* sc = (LAS float*)c.lds;
;     LAS float* red = (LAS float*)(c.lds + 40960);
;     for (int i = c.tid; i < 5 * DM; i += 512) { const int r = i >> 11, k = i & 2047; const float v = r < 4 ? INP(1)[r * DM + k] : INP(3)[k]; sc[i] = silu_(v); }
;     __syncthreads();
.LBB0_108:
	v_lshlrev_b32_e32 v3, 2, v2
	global_load_dword v16, v3, s[26:27]
	v_add_u32_e32 v3, 0x800, v3
	global_load_dword v17, v3, s[26:27]
	v_add_u32_e32 v3, 0x800, v3
	global_load_dword v18, v3, s[26:27]
	v_add_u32_e32 v3, 0x800, v3
	global_load_dword v19, v3, s[26:27]
	v_add_u32_e32 v3, 0x800, v3
	global_load_dword v20, v3, s[26:27]
	v_add_u32_e32 v3, 0x800, v3
	global_load_dword v21, v3, s[26:27]
	v_add_u32_e32 v3, 0x800, v3
	global_load_dword v22, v3, s[26:27]
	v_add_u32_e32 v3, 0x800, v3
	global_load_dword v23, v3, s[26:27]
	v_add_u32_e32 v3, 0x800, v3
	global_load_dword v24, v3, s[26:27]
	v_add_u32_e32 v3, 0x800, v3
	global_load_dword v25, v3, s[26:27]
	v_add_u32_e32 v3, 0x800, v3
	global_load_dword v26, v3, s[26:27]
	v_add_u32_e32 v3, 0x800, v3
	global_load_dword v27, v3, s[26:27]
	v_add_u32_e32 v3, 0x800, v3
	global_load_dword v28, v3, s[26:27]
	v_add_u32_e32 v3, 0x800, v3
	global_load_dword v29, v3, s[26:27]
	v_add_u32_e32 v3, 0x800, v3
	global_load_dword v30, v3, s[26:27]
	v_add_u32_e32 v3, 0x800, v3
	global_load_dword v31, v3, s[26:27]
	v_lshlrev_b32_e32 v3, 2, v2
	global_load_dword v32, v3, s[16:17]
	v_add_u32_e32 v3, 0x800, v3
	global_load_dword v33, v3, s[16:17]
	v_add_u32_e32 v3, 0x800, v3
	global_load_dword v34, v3, s[16:17]
	v_add_u32_e32 v3, 0x800, v3
	global_load_dword v35, v3, s[16:17]
	s_waitcnt vmcnt(19)
	v_mul_f32_e32 v8, 0xbfb8aa3b, v16
	v_exp_f32_e32 v8, v8
	s_nop 0
	v_add_f32_e32 v8, 1.0, v8
	v_div_scale_f32 v9, s[10:11], v8, v8, 1.0
	v_rcp_f32_e32 v10, v9
	v_div_scale_f32 v11, vcc, 1.0, v8, 1.0
	v_fma_f32 v12, -v9, v10, 1.0
	v_fmac_f32_e32 v10, v12, v10
	v_mul_f32_e32 v12, v11, v10
	v_fma_f32 v13, -v9, v12, v11
	v_fmac_f32_e32 v12, v13, v10
	v_fma_f32 v9, -v9, v12, v11
	v_div_fmas_f32 v9, v9, v10, v12
	v_div_fixup_f32 v8, v9, v8, 1.0
	v_mul_f32_e32 v16, v16, v8
	ds_write_b32 v1, v16
	s_waitcnt vmcnt(18)
	v_mul_f32_e32 v8, 0xbfb8aa3b, v17
	v_exp_f32_e32 v8, v8
	s_nop 0
	v_add_f32_e32 v8, 1.0, v8
	v_div_scale_f32 v9, s[10:11], v8, v8, 1.0
	v_rcp_f32_e32 v10, v9
	v_div_scale_f32 v11, vcc, 1.0, v8, 1.0
	v_fma_f32 v12, -v9, v10, 1.0
	v_fmac_f32_e32 v10, v12, v10
	v_mul_f32_e32 v12, v11, v10
	v_fma_f32 v13, -v9, v12, v11
	v_fmac_f32_e32 v12, v13, v10
	v_fma_f32 v9, -v9, v12, v11
	v_div_fmas_f32 v9, v9, v10, v12
	v_div_fixup_f32 v8, v9, v8, 1.0
	v_mul_f32_e32 v17, v17, v8
	ds_write_b32 v1, v17 offset:2048
	s_waitcnt vmcnt(17)
	v_mul_f32_e32 v8, 0xbfb8aa3b, v18
	v_exp_f32_e32 v8, v8
	s_nop 0
	v_add_f32_e32 v8, 1.0, v8
	v_div_scale_f32 v9, s[10:11], v8, v8, 1.0
	v_rcp_f32_e32 v10, v9
	v_div_scale_f32 v11, vcc, 1.0, v8, 1.0
	v_fma_f32 v12, -v9, v10, 1.0
	v_fmac_f32_e32 v10, v12, v10
	v_mul_f32_e32 v12, v11, v10
	v_fma_f32 v13, -v9, v12, v11
	v_fmac_f32_e32 v12, v13, v10
	v_fma_f32 v9, -v9, v12, v11
	v_div_fmas_f32 v9, v9, v10, v12
	v_div_fixup_f32 v8, v9, v8, 1.0
	v_mul_f32_e32 v18, v18, v8
	ds_write_b32 v1, v18 offset:4096
	s_waitcnt vmcnt(16)
	v_mul_f32_e32 v8, 0xbfb8aa3b, v19
	v_exp_f32_e32 v8, v8
	s_nop 0
	v_add_f32_e32 v8, 1.0, v8
	v_div_scale_f32 v9, s[10:11], v8, v8, 1.0
	v_rcp_f32_e32 v10, v9
	v_div_scale_f32 v11, vcc, 1.0, v8, 1.0
	v_fma_f32 v12, -v9, v10, 1.0
	v_fmac_f32_e32 v10, v12, v10
	v_mul_f32_e32 v12, v11, v10
	v_fma_f32 v13, -v9, v12, v11
	v_fmac_f32_e32 v12, v13, v10
	v_fma_f32 v9, -v9, v12, v11
	v_div_fmas_f32 v9, v9, v10, v12
	v_div_fixup_f32 v8, v9, v8, 1.0
	v_mul_f32_e32 v19, v19, v8
	ds_write_b32 v1, v19 offset:6144
	s_waitcnt vmcnt(15)
	v_mul_f32_e32 v8, 0xbfb8aa3b, v20
	v_exp_f32_e32 v8, v8
	s_nop 0
	v_add_f32_e32 v8, 1.0, v8
	v_div_scale_f32 v9, s[10:11], v8, v8, 1.0
	v_rcp_f32_e32 v10, v9
	v_div_scale_f32 v11, vcc, 1.0, v8, 1.0
	v_fma_f32 v12, -v9, v10, 1.0
	v_fmac_f32_e32 v10, v12, v10
	v_mul_f32_e32 v12, v11, v10
	v_fma_f32 v13, -v9, v12, v11
	v_fmac_f32_e32 v12, v13, v10
	v_fma_f32 v9, -v9, v12, v11
	v_div_fmas_f32 v9, v9, v10, v12
	v_div_fixup_f32 v8, v9, v8, 1.0
	v_mul_f32_e32 v20, v20, v8
	ds_write_b32 v1, v20 offset:8192
	s_waitcnt vmcnt(14)
	v_mul_f32_e32 v8, 0xbfb8aa3b, v21
	v_exp_f32_e32 v8, v8
	s_nop 0
	v_add_f32_e32 v8, 1.0, v8
	v_div_scale_f32 v9, s[10:11], v8, v8, 1.0
	v_rcp_f32_e32 v10, v9
	v_div_scale_f32 v11, vcc, 1.0, v8, 1.0
	v_fma_f32 v12, -v9, v10, 1.0
	v_fmac_f32_e32 v10, v12, v10
	v_mul_f32_e32 v12, v11, v10
	v_fma_f32 v13, -v9, v12, v11
	v_fmac_f32_e32 v12, v13, v10
	v_fma_f32 v9, -v9, v12, v11
	v_div_fmas_f32 v9, v9, v10, v12
	v_div_fixup_f32 v8, v9, v8, 1.0
	v_mul_f32_e32 v21, v21, v8
	ds_write_b32 v1, v21 offset:10240
	s_waitcnt vmcnt(13)
	v_mul_f32_e32 v8, 0xbfb8aa3b, v22
	v_exp_f32_e32 v8, v8
	s_nop 0
	v_add_f32_e32 v8, 1.0, v8
	v_div_scale_f32 v9, s[10:11], v8, v8, 1.0
	v_rcp_f32_e32 v10, v9
	v_div_scale_f32 v11, vcc, 1.0, v8, 1.0
	v_fma_f32 v12, -v9, v10, 1.0
	v_fmac_f32_e32 v10, v12, v10
	v_mul_f32_e32 v12, v11, v10
	v_fma_f32 v13, -v9, v12, v11
	v_fmac_f32_e32 v12, v13, v10
	v_fma_f32 v9, -v9, v12, v11
	v_div_fmas_f32 v9, v9, v10, v12
	v_div_fixup_f32 v8, v9, v8, 1.0
	v_mul_f32_e32 v22, v22, v8
	ds_write_b32 v1, v22 offset:12288
	s_waitcnt vmcnt(12)
	v_mul_f32_e32 v8, 0xbfb8aa3b, v23
	v_exp_f32_e32 v8, v8
	s_nop 0
	v_add_f32_e32 v8, 1.0, v8
	v_div_scale_f32 v9, s[10:11], v8, v8, 1.0
	v_rcp_f32_e32 v10, v9
	v_div_scale_f32 v11, vcc, 1.0, v8, 1.0
	v_fma_f32 v12, -v9, v10, 1.0
	v_fmac_f32_e32 v10, v12, v10
	v_mul_f32_e32 v12, v11, v10
	v_fma_f32 v13, -v9, v12, v11
	v_fmac_f32_e32 v12, v13, v10
	v_fma_f32 v9, -v9, v12, v11
	v_div_fmas_f32 v9, v9, v10, v12
	v_div_fixup_f32 v8, v9, v8, 1.0
	v_mul_f32_e32 v23, v23, v8
	ds_write_b32 v1, v23 offset:14336
	s_waitcnt vmcnt(11)
; #define LAS __attribute__((address_space(3)))
; __device__ __forceinline__ float sigmoid_(float x) { return 1.f / (1.f + __expf(-x)); }
; __device__ __forceinline__ float silu_(float x) { return x * sigmoid_(x); }
; __device__ __forceinline__ void mod_items(const Args& a, const Ctx& c0, int l) {
;     ...
;     __syncthreads();
;     LAS float* sc = (LAS float*)c.lds;
;     LAS float* red = (LAS float*)(c.lds + 40960);
;     for (int i = c.tid; i < 5 * DM; i += 512) { const int r = i >> 11, k = i & 2047; const float v = r < 4 ? INP(1)[r * DM + k] : INP(3)[k]; sc[i] = silu_(v); }
;     __syncthreads();
	v_mul_f32_e32 v8, 0xbfb8aa3b, v24
	v_exp_f32_e32 v8, v8
	s_nop 0
	v_add_f32_e32 v8, 1.0, v8
	v_div_scale_f32 v9, s[10:11], v8, v8, 1.0
	v_rcp_f32_e32 v10, v9
	v_div_scale_f32 v11, vcc, 1.0, v8, 1.0
	v_fma_f32 v12, -v9, v10, 1.0
	v_fmac_f32_e32 v10, v12, v10
	v_mul_f32_e32 v12, v11, v10
	v_fma_f32 v13, -v9, v12, v11
	v_fmac_f32_e32 v12, v13, v10
	v_fma_f32 v9, -v9, v12, v11
	v_div_fmas_f32 v9, v9, v10, v12
	v_div_fixup_f32 v8, v9, v8, 1.0
	v_mul_f32_e32 v24, v24, v8
	ds_write_b32 v1, v24 offset:16384
	s_waitcnt vmcnt(10)
	v_mul_f32_e32 v8, 0xbfb8aa3b, v25
	v_exp_f32_e32 v8, v8
	s_nop 0
	v_add_f32_e32 v8, 1.0, v8
	v_div_scale_f32 v9, s[10:11], v8, v8, 1.0
	v_rcp_f32_e32 v10, v9
	v_div_scale_f32 v11, vcc, 1.0, v8, 1.0
	v_fma_f32 v12, -v9, v10, 1.0
	v_fmac_f32_e32 v10, v12, v10
	v_mul_f32_e32 v12, v11, v10
	v_fma_f32 v13, -v9, v12, v11
	v_fmac_f32_e32 v12, v13, v10
	v_fma_f32 v9, -v9, v12, v11
	v_div_fmas_f32 v9, v9, v10, v12
	v_div_fixup_f32 v8, v9, v8, 1.0
	v_mul_f32_e32 v25, v25, v8
	ds_write_b32 v1, v25 offset:18432
	s_waitcnt vmcnt(9)
	v_mul_f32_e32 v8, 0xbfb8aa3b, v26
	v_exp_f32_e32 v8, v8
	s_nop 0
	v_add_f32_e32 v8, 1.0, v8
	v_div_scale_f32 v9, s[10:11], v8, v8, 1.0
	v_rcp_f32_e32 v10, v9
	v_div_scale_f32 v11, vcc, 1.0, v8, 1.0
	v_fma_f32 v12, -v9, v10, 1.0
	v_fmac_f32_e32 v10, v12, v10
	v_mul_f32_e32 v12, v11, v10
	v_fma_f32 v13, -v9, v12, v11
	v_fmac_f32_e32 v12, v13, v10
	v_fma_f32 v9, -v9, v12, v11
	v_div_fmas_f32 v9, v9, v10, v12
	v_div_fixup_f32 v8, v9, v8, 1.0
	v_mul_f32_e32 v26, v26, v8
	ds_write_b32 v1, v26 offset:20480
	s_waitcnt vmcnt(8)
	v_mul_f32_e32 v8, 0xbfb8aa3b, v27
	v_exp_f32_e32 v8, v8
	s_nop 0
	v_add_f32_e32 v8, 1.0, v8
	v_div_scale_f32 v9, s[10:11], v8, v8, 1.0
	v_rcp_f32_e32 v10, v9
	v_div_scale_f32 v11, vcc, 1.0, v8, 1.0
	v_fma_f32 v12, -v9, v10, 1.0
	v_fmac_f32_e32 v10, v12, v10
	v_mul_f32_e32 v12, v11, v10
	v_fma_f32 v13, -v9, v12, v11
	v_fmac_f32_e32 v12, v13, v10
	v_fma_f32 v9, -v9, v12, v11
	v_div_fmas_f32 v9, v9, v10, v12
	v_div_fixup_f32 v8, v9, v8, 1.0
	v_mul_f32_e32 v27, v27, v8
	ds_write_b32 v1, v27 offset:22528
	s_waitcnt vmcnt(7)
	v_mul_f32_e32 v8, 0xbfb8aa3b, v28
	v_exp_f32_e32 v8, v8
	s_nop 0
	v_add_f32_e32 v8, 1.0, v8
	v_div_scale_f32 v9, s[10:11], v8, v8, 1.0
	v_rcp_f32_e32 v10, v9
	v_div_scale_f32 v11, vcc, 1.0, v8, 1.0
	v_fma_f32 v12, -v9, v10, 1.0
	v_fmac_f32_e32 v10, v12, v10
	v_mul_f32_e32 v12, v11, v10
	v_fma_f32 v13, -v9, v12, v11
	v_fmac_f32_e32 v12, v13, v10
	v_fma_f32 v9, -v9, v12, v11
	v_div_fmas_f32 v9, v9, v10, v12
	v_div_fixup_f32 v8, v9, v8, 1.0
	v_mul_f32_e32 v28, v28, v8
	ds_write_b32 v1, v28 offset:24576
	s_waitcnt vmcnt(6)
	v_mul_f32_e32 v8, 0xbfb8aa3b, v29
	v_exp_f32_e32 v8, v8
	s_nop 0
	v_add_f32_e32 v8, 1.0, v8
	v_div_scale_f32 v9, s[10:11], v8, v8, 1.0
	v_rcp_f32_e32 v10, v9
	v_div_scale_f32 v11, vcc, 1.0, v8, 1.0
	v_fma_f32 v12, -v9, v10, 1.0
	v_fmac_f32_e32 v10, v12, v10
	v_mul_f32_e32 v12, v11, v10
	v_fma_f32 v13, -v9, v12, v11
	v_fmac_f32_e32 v12, v13, v10
	v_fma_f32 v9, -v9, v12, v11
	v_div_fmas_f32 v9, v9, v10, v12
	v_div_fixup_f32 v8, v9, v8, 1.0
	v_mul_f32_e32 v29, v29, v8
	ds_write_b32 v1, v29 offset:26624
	s_waitcnt vmcnt(5)
	v_mul_f32_e32 v8, 0xbfb8aa3b, v30
	v_exp_f32_e32 v8, v8
	s_nop 0
	v_add_f32_e32 v8, 1.0, v8
	v_div_scale_f32 v9, s[10:11], v8, v8, 1.0
	v_rcp_f32_e32 v10, v9
	v_div_scale_f32 v11, vcc, 1.0, v8, 1.0
	v_fma_f32 v12, -v9, v10, 1.0
	v_fmac_f32_e32 v10, v12, v10
	v_mul_f32_e32 v12, v11, v10
	v_fma_f32 v13, -v9, v12, v11
	v_fmac_f32_e32 v12, v13, v10
	v_fma_f32 v9, -v9, v12, v11
	v_div_fmas_f32 v9, v9, v10, v12
	v_div_fixup_f32 v8, v9, v8, 1.0
	v_mul_f32_e32 v30, v30, v8
	ds_write_b32 v1, v30 offset:28672
	s_waitcnt vmcnt(4)
	v_mul_f32_e32 v8, 0xbfb8aa3b, v31
	v_exp_f32_e32 v8, v8
	s_nop 0
	v_add_f32_e32 v8, 1.0, v8
	v_div_scale_f32 v9, s[10:11], v8, v8, 1.0
	v_rcp_f32_e32 v10, v9
	v_div_scale_f32 v11, vcc, 1.0, v8, 1.0
	v_fma_f32 v12, -v9, v10, 1.0
	v_fmac_f32_e32 v10, v12, v10
	v_mul_f32_e32 v12, v11, v10
	v_fma_f32 v13, -v9, v12, v11
	v_fmac_f32_e32 v12, v13, v10
	v_fma_f32 v9, -v9, v12, v11
	v_div_fmas_f32 v9, v9, v10, v12
	v_div_fixup_f32 v8, v9, v8, 1.0
	v_mul_f32_e32 v31, v31, v8
	ds_write_b32 v1, v31 offset:30720
	s_waitcnt vmcnt(3)
	v_mul_f32_e32 v8, 0xbfb8aa3b, v32
	v_exp_f32_e32 v8, v8
	s_nop 0
	v_add_f32_e32 v8, 1.0, v8
	v_div_scale_f32 v9, s[10:11], v8, v8, 1.0
	v_rcp_f32_e32 v10, v9
	v_div_scale_f32 v11, vcc, 1.0, v8, 1.0
	v_fma_f32 v12, -v9, v10, 1.0
	v_fmac_f32_e32 v10, v12, v10
	v_mul_f32_e32 v12, v11, v10
	v_fma_f32 v13, -v9, v12, v11
	v_fmac_f32_e32 v12, v13, v10
	v_fma_f32 v9, -v9, v12, v11
	v_div_fmas_f32 v9, v9, v10, v12
	v_div_fixup_f32 v8, v9, v8, 1.0
	v_mul_f32_e32 v32, v32, v8
	ds_write_b32 v1, v32 offset:32768
	s_waitcnt vmcnt(2)
	v_mul_f32_e32 v8, 0xbfb8aa3b, v33
	v_exp_f32_e32 v8, v8
	s_nop 0
	v_add_f32_e32 v8, 1.0, v8
	v_div_scale_f32 v9, s[10:11], v8, v8, 1.0
	v_rcp_f32_e32 v10, v9
	v_div_scale_f32 v11, vcc, 1.0, v8, 1.0
	v_fma_f32 v12, -v9, v10, 1.0
	v_fmac_f32_e32 v10, v12, v10
	v_mul_f32_e32 v12, v11, v10
	v_fma_f32 v13, -v9, v12, v11
	v_fmac_f32_e32 v12, v13, v10
	v_fma_f32 v9, -v9, v12, v11
	v_div_fmas_f32 v9, v9, v10, v12
	v_div_fixup_f32 v8, v9, v8, 1.0
	v_mul_f32_e32 v33, v33, v8
	ds_write_b32 v1, v33 offset:34816
	s_waitcnt vmcnt(1)
	v_mul_f32_e32 v8, 0xbfb8aa3b, v34
	v_exp_f32_e32 v8, v8
	s_nop 0
	v_add_f32_e32 v8, 1.0, v8
	v_div_scale_f32 v9, s[10:11], v8, v8, 1.0
	v_rcp_f32_e32 v10, v9
	v_div_scale_f32 v11, vcc, 1.0, v8, 1.0
	v_fma_f32 v12, -v9, v10, 1.0
	v_fmac_f32_e32 v10, v12, v10
	v_mul_f32_e32 v12, v11, v10
	v_fma_f32 v13, -v9, v12, v11
	v_fmac_f32_e32 v12, v13, v10
	v_fma_f32 v9, -v9, v12, v11
	v_div_fmas_f32 v9, v9, v10, v12
	v_div_fixup_f32 v8, v9, v8, 1.0
	v_mul_f32_e32 v34, v34, v8
	ds_write_b32 v1, v34 offset:36864
	s_waitcnt vmcnt(0)
	v_mul_f32_e32 v8, 0xbfb8aa3b, v35
	v_exp_f32_e32 v8, v8
	s_nop 0
	v_add_f32_e32 v8, 1.0, v8
	v_div_scale_f32 v9, s[10:11], v8, v8, 1.0
	v_rcp_f32_e32 v10, v9
	v_div_scale_f32 v11, vcc, 1.0, v8, 1.0
	v_fma_f32 v12, -v9, v10, 1.0
	v_fmac_f32_e32 v10, v12, v10
	v_mul_f32_e32 v12, v11, v10
	v_fma_f32 v13, -v9, v12, v11
	v_fmac_f32_e32 v12, v13, v10
	v_fma_f32 v9, -v9, v12, v11
	v_div_fmas_f32 v9, v9, v10, v12
	v_div_fixup_f32 v8, v9, v8, 1.0
	v_mul_f32_e32 v35, v35, v8
	ds_write_b32 v1, v35 offset:38912

; #define LAS __attribute__((address_space(3)))
; __device__ __forceinline__ float sigmoid_(float x) { return 1.f / (1.f + __expf(-x)); }
; __device__ __forceinline__ float silu_(float x) { return x * sigmoid_(x); }
; __device__ __forceinline__ void mod_items(const Args& a, const Ctx& c0, int l) {
;     ...
;     __syncthreads();
;     LAS float* sc = (LAS float*)c.lds;
;     LAS float* red = (LAS float*)(c.lds + 40960);
;     for (int i = c.tid; i < 5 * DM; i += 512) { const int r = i >> 11, k = i & 2047; const float v = r < 4 ? INP(1)[r * DM + k] : INP(3)[k]; sc[i] = silu_(v); }
;     __syncthreads();
.LBB0_1237:
	v_lshlrev_b32_e32 v3, 2, v2
	global_load_dword v16, v3, s[42:43]
	v_add_u32_e32 v3, 0x800, v3
	global_load_dword v17, v3, s[42:43]
	v_add_u32_e32 v3, 0x800, v3
	global_load_dword v18, v3, s[42:43]
	v_add_u32_e32 v3, 0x800, v3
	global_load_dword v19, v3, s[42:43]
	v_add_u32_e32 v3, 0x800, v3
	global_load_dword v20, v3, s[42:43]
	v_add_u32_e32 v3, 0x800, v3
	global_load_dword v21, v3, s[42:43]
	v_add_u32_e32 v3, 0x800, v3
	global_load_dword v22, v3, s[42:43]
	v_add_u32_e32 v3, 0x800, v3
	global_load_dword v23, v3, s[42:43]
	v_add_u32_e32 v3, 0x800, v3
	global_load_dword v24, v3, s[42:43]
	v_add_u32_e32 v3, 0x800, v3
	global_load_dword v25, v3, s[42:43]
	v_add_u32_e32 v3, 0x800, v3
	global_load_dword v26, v3, s[42:43]
	v_add_u32_e32 v3, 0x800, v3
	global_load_dword v27, v3, s[42:43]
	v_add_u32_e32 v3, 0x800, v3
	global_load_dword v28, v3, s[42:43]
	v_add_u32_e32 v3, 0x800, v3
	global_load_dword v29, v3, s[42:43]
	v_add_u32_e32 v3, 0x800, v3
	global_load_dword v30, v3, s[42:43]
	v_add_u32_e32 v3, 0x800, v3
	global_load_dword v31, v3, s[42:43]
	v_lshlrev_b32_e32 v3, 2, v2
	global_load_dword v32, v3, s[46:47]
	v_add_u32_e32 v3, 0x800, v3
	global_load_dword v33, v3, s[46:47]
	v_add_u32_e32 v3, 0x800, v3
	global_load_dword v34, v3, s[46:47]
	v_add_u32_e32 v3, 0x800, v3
	global_load_dword v35, v3, s[46:47]
	s_waitcnt vmcnt(19)
	v_mul_f32_e32 v8, 0xbfb8aa3b, v16
	v_exp_f32_e32 v8, v8
	s_nop 0
	v_add_f32_e32 v8, 1.0, v8
	v_div_scale_f32 v9, s[10:11], v8, v8, 1.0
	v_rcp_f32_e32 v10, v9
	v_div_scale_f32 v11, vcc, 1.0, v8, 1.0
	v_fma_f32 v12, -v9, v10, 1.0
	v_fmac_f32_e32 v10, v12, v10
	v_mul_f32_e32 v12, v11, v10
	v_fma_f32 v13, -v9, v12, v11
	v_fmac_f32_e32 v12, v13, v10
	v_fma_f32 v9, -v9, v12, v11
	v_div_fmas_f32 v9, v9, v10, v12
	v_div_fixup_f32 v8, v9, v8, 1.0
	v_mul_f32_e32 v16, v16, v8
	ds_write_b32 v6, v16
	s_waitcnt vmcnt(18)
	v_mul_f32_e32 v8, 0xbfb8aa3b, v17
	v_exp_f32_e32 v8, v8
	s_nop 0
	v_add_f32_e32 v8, 1.0, v8
	v_div_scale_f32 v9, s[10:11], v8, v8, 1.0
	v_rcp_f32_e32 v10, v9
	v_div_scale_f32 v11, vcc, 1.0, v8, 1.0
	v_fma_f32 v12, -v9, v10, 1.0
	v_fmac_f32_e32 v10, v12, v10
	v_mul_f32_e32 v12, v11, v10
	v_fma_f32 v13, -v9, v12, v11
	v_fmac_f32_e32 v12, v13, v10
	v_fma_f32 v9, -v9, v12, v11
	v_div_fmas_f32 v9, v9, v10, v12
	v_div_fixup_f32 v8, v9, v8, 1.0
	v_mul_f32_e32 v17, v17, v8
	ds_write_b32 v6, v17 offset:2048
	s_waitcnt vmcnt(17)
	v_mul_f32_e32 v8, 0xbfb8aa3b, v18
	v_exp_f32_e32 v8, v8
	s_nop 0
	v_add_f32_e32 v8, 1.0, v8
	v_div_scale_f32 v9, s[10:11], v8, v8, 1.0
	v_rcp_f32_e32 v10, v9
	v_div_scale_f32 v11, vcc, 1.0, v8, 1.0
	v_fma_f32 v12, -v9, v10, 1.0
	v_fmac_f32_e32 v10, v12, v10
	v_mul_f32_e32 v12, v11, v10
	v_fma_f32 v13, -v9, v12, v11
	v_fmac_f32_e32 v12, v13, v10
	v_fma_f32 v9, -v9, v12, v11
	v_div_fmas_f32 v9, v9, v10, v12
	v_div_fixup_f32 v8, v9, v8, 1.0
	v_mul_f32_e32 v18, v18, v8
	ds_write_b32 v6, v18 offset:4096
	s_waitcnt vmcnt(16)
	v_mul_f32_e32 v8, 0xbfb8aa3b, v19
	v_exp_f32_e32 v8, v8
	s_nop 0
	v_add_f32_e32 v8, 1.0, v8
	v_div_scale_f32 v9, s[10:11], v8, v8, 1.0
	v_rcp_f32_e32 v10, v9
	v_div_scale_f32 v11, vcc, 1.0, v8, 1.0
	v_fma_f32 v12, -v9, v10, 1.0
	v_fmac_f32_e32 v10, v12, v10
	v_mul_f32_e32 v12, v11, v10
	v_fma_f32 v13, -v9, v12, v11
	v_fmac_f32_e32 v12, v13, v10
	v_fma_f32 v9, -v9, v12, v11
	v_div_fmas_f32 v9, v9, v10, v12
	v_div_fixup_f32 v8, v9, v8, 1.0
	v_mul_f32_e32 v19, v19, v8
	ds_write_b32 v6, v19 offset:6144
	s_waitcnt vmcnt(15)
	v_mul_f32_e32 v8, 0xbfb8aa3b, v20
	v_exp_f32_e32 v8, v8
	s_nop 0
	v_add_f32_e32 v8, 1.0, v8
	v_div_scale_f32 v9, s[10:11], v8, v8, 1.0
	v_rcp_f32_e32 v10, v9
	v_div_scale_f32 v11, vcc, 1.0, v8, 1.0
	v_fma_f32 v12, -v9, v10, 1.0
	v_fmac_f32_e32 v10, v12, v10
	v_mul_f32_e32 v12, v11, v10
	v_fma_f32 v13, -v9, v12, v11
	v_fmac_f32_e32 v12, v13, v10
	v_fma_f32 v9, -v9, v12, v11
	v_div_fmas_f32 v9, v9, v10, v12
	v_div_fixup_f32 v8, v9, v8, 1.0
	v_mul_f32_e32 v20, v20, v8
	ds_write_b32 v6, v20 offset:8192
	s_waitcnt vmcnt(14)
	v_mul_f32_e32 v8, 0xbfb8aa3b, v21
	v_exp_f32_e32 v8, v8
	s_nop 0
	v_add_f32_e32 v8, 1.0, v8
	v_div_scale_f32 v9, s[10:11], v8, v8, 1.0
	v_rcp_f32_e32 v10, v9
	v_div_scale_f32 v11, vcc, 1.0, v8, 1.0
	v_fma_f32 v12, -v9, v10, 1.0
	v_fmac_f32_e32 v10, v12, v10
	v_mul_f32_e32 v12, v11, v10
	v_fma_f32 v13, -v9, v12, v11
	v_fmac_f32_e32 v12, v13, v10
	v_fma_f32 v9, -v9, v12, v11
	v_div_fmas_f32 v9, v9, v10, v12
	v_div_fixup_f32 v8, v9, v8, 1.0
	v_mul_f32_e32 v21, v21, v8
	ds_write_b32 v6, v21 offset:10240
	s_waitcnt vmcnt(13)
	v_mul_f32_e32 v8, 0xbfb8aa3b, v22
	v_exp_f32_e32 v8, v8
	s_nop 0
	v_add_f32_e32 v8, 1.0, v8
	v_div_scale_f32 v9, s[10:11], v8, v8, 1.0
	v_rcp_f32_e32 v10, v9
	v_div_scale_f32 v11, vcc, 1.0, v8, 1.0
	v_fma_f32 v12, -v9, v10, 1.0
	v_fmac_f32_e32 v10, v12, v10
	v_mul_f32_e32 v12, v11, v10
	v_fma_f32 v13, -v9, v12, v11
	v_fmac_f32_e32 v12, v13, v10
	v_fma_f32 v9, -v9, v12, v11
	v_div_fmas_f32 v9, v9, v10, v12
	v_div_fixup_f32 v8, v9, v8, 1.0
	v_mul_f32_e32 v22, v22, v8
	ds_write_b32 v6, v22 offset:12288
	s_waitcnt vmcnt(12)
	v_mul_f32_e32 v8, 0xbfb8aa3b, v23
	v_exp_f32_e32 v8, v8
	s_nop 0
	v_add_f32_e32 v8, 1.0, v8
	v_div_scale_f32 v9, s[10:11], v8, v8, 1.0
	v_rcp_f32_e32 v10, v9
	v_div_scale_f32 v11, vcc, 1.0, v8, 1.0
	v_fma_f32 v12, -v9, v10, 1.0
	v_fmac_f32_e32 v10, v12, v10
	v_mul_f32_e32 v12, v11, v10
	v_fma_f32 v13, -v9, v12, v11
	v_fmac_f32_e32 v12, v13, v10
	v_fma_f32 v9, -v9, v12, v11
	v_div_fmas_f32 v9, v9, v10, v12
	v_div_fixup_f32 v8, v9, v8, 1.0
	v_mul_f32_e32 v23, v23, v8
	ds_write_b32 v6, v23 offset:14336
	s_waitcnt vmcnt(11)
; #define LAS __attribute__((address_space(3)))
; __device__ __forceinline__ float sigmoid_(float x) { return 1.f / (1.f + __expf(-x)); }
; __device__ __forceinline__ float silu_(float x) { return x * sigmoid_(x); }
; __device__ __forceinline__ void mod_items(const Args& a, const Ctx& c0, int l) {
;     ...
;     __syncthreads();
;     LAS float* sc = (LAS float*)c.lds;
;     LAS float* red = (LAS float*)(c.lds + 40960);
;     for (int i = c.tid; i < 5 * DM; i += 512) { const int r = i >> 11, k = i & 2047; const float v = r < 4 ? INP(1)[r * DM + k] : INP(3)[k]; sc[i] = silu_(v); }
;     __syncthreads();
	v_mul_f32_e32 v8, 0xbfb8aa3b, v24
	v_exp_f32_e32 v8, v8
	s_nop 0
	v_add_f32_e32 v8, 1.0, v8
	v_div_scale_f32 v9, s[10:11], v8, v8, 1.0
	v_rcp_f32_e32 v10, v9
	v_div_scale_f32 v11, vcc, 1.0, v8, 1.0
	v_fma_f32 v12, -v9, v10, 1.0
	v_fmac_f32_e32 v10, v12, v10
	v_mul_f32_e32 v12, v11, v10
	v_fma_f32 v13, -v9, v12, v11
	v_fmac_f32_e32 v12, v13, v10
	v_fma_f32 v9, -v9, v12, v11
	v_div_fmas_f32 v9, v9, v10, v12
	v_div_fixup_f32 v8, v9, v8, 1.0
	v_mul_f32_e32 v24, v24, v8
	ds_write_b32 v6, v24 offset:16384
	s_waitcnt vmcnt(10)
	v_mul_f32_e32 v8, 0xbfb8aa3b, v25
	v_exp_f32_e32 v8, v8
	s_nop 0
	v_add_f32_e32 v8, 1.0, v8
	v_div_scale_f32 v9, s[10:11], v8, v8, 1.0
	v_rcp_f32_e32 v10, v9
	v_div_scale_f32 v11, vcc, 1.0, v8, 1.0
	v_fma_f32 v12, -v9, v10, 1.0
	v_fmac_f32_e32 v10, v12, v10
	v_mul_f32_e32 v12, v11, v10
	v_fma_f32 v13, -v9, v12, v11
	v_fmac_f32_e32 v12, v13, v10
	v_fma_f32 v9, -v9, v12, v11
	v_div_fmas_f32 v9, v9, v10, v12
	v_div_fixup_f32 v8, v9, v8, 1.0
	v_mul_f32_e32 v25, v25, v8
	ds_write_b32 v6, v25 offset:18432
	s_waitcnt vmcnt(9)
	v_mul_f32_e32 v8, 0xbfb8aa3b, v26
	v_exp_f32_e32 v8, v8
	s_nop 0
	v_add_f32_e32 v8, 1.0, v8
	v_div_scale_f32 v9, s[10:11], v8, v8, 1.0
	v_rcp_f32_e32 v10, v9
	v_div_scale_f32 v11, vcc, 1.0, v8, 1.0
	v_fma_f32 v12, -v9, v10, 1.0
	v_fmac_f32_e32 v10, v12, v10
	v_mul_f32_e32 v12, v11, v10
	v_fma_f32 v13, -v9, v12, v11
	v_fmac_f32_e32 v12, v13, v10
	v_fma_f32 v9, -v9, v12, v11
	v_div_fmas_f32 v9, v9, v10, v12
	v_div_fixup_f32 v8, v9, v8, 1.0
	v_mul_f32_e32 v26, v26, v8
	ds_write_b32 v6, v26 offset:20480
	s_waitcnt vmcnt(8)
	v_mul_f32_e32 v8, 0xbfb8aa3b, v27
	v_exp_f32_e32 v8, v8
	s_nop 0
	v_add_f32_e32 v8, 1.0, v8
	v_div_scale_f32 v9, s[10:11], v8, v8, 1.0
	v_rcp_f32_e32 v10, v9
	v_div_scale_f32 v11, vcc, 1.0, v8, 1.0
	v_fma_f32 v12, -v9, v10, 1.0
	v_fmac_f32_e32 v10, v12, v10
	v_mul_f32_e32 v12, v11, v10
	v_fma_f32 v13, -v9, v12, v11
	v_fmac_f32_e32 v12, v13, v10
	v_fma_f32 v9, -v9, v12, v11
	v_div_fmas_f32 v9, v9, v10, v12
	v_div_fixup_f32 v8, v9, v8, 1.0
	v_mul_f32_e32 v27, v27, v8
	ds_write_b32 v6, v27 offset:22528
	s_waitcnt vmcnt(7)
	v_mul_f32_e32 v8, 0xbfb8aa3b, v28
	v_exp_f32_e32 v8, v8
	s_nop 0
	v_add_f32_e32 v8, 1.0, v8
	v_div_scale_f32 v9, s[10:11], v8, v8, 1.0
	v_rcp_f32_e32 v10, v9
	v_div_scale_f32 v11, vcc, 1.0, v8, 1.0
	v_fma_f32 v12, -v9, v10, 1.0
	v_fmac_f32_e32 v10, v12, v10
	v_mul_f32_e32 v12, v11, v10
	v_fma_f32 v13, -v9, v12, v11
	v_fmac_f32_e32 v12, v13, v10
	v_fma_f32 v9, -v9, v12, v11
	v_div_fmas_f32 v9, v9, v10, v12
	v_div_fixup_f32 v8, v9, v8, 1.0
	v_mul_f32_e32 v28, v28, v8
	ds_write_b32 v6, v28 offset:24576
	s_waitcnt vmcnt(6)
	v_mul_f32_e32 v8, 0xbfb8aa3b, v29
	v_exp_f32_e32 v8, v8
	s_nop 0
	v_add_f32_e32 v8, 1.0, v8
	v_div_scale_f32 v9, s[10:11], v8, v8, 1.0
	v_rcp_f32_e32 v10, v9
	v_div_scale_f32 v11, vcc, 1.0, v8, 1.0
	v_fma_f32 v12, -v9, v10, 1.0
	v_fmac_f32_e32 v10, v12, v10
	v_mul_f32_e32 v12, v11, v10
	v_fma_f32 v13, -v9, v12, v11
	v_fmac_f32_e32 v12, v13, v10
	v_fma_f32 v9, -v9, v12, v11
	v_div_fmas_f32 v9, v9, v10, v12
	v_div_fixup_f32 v8, v9, v8, 1.0
	v_mul_f32_e32 v29, v29, v8
	ds_write_b32 v6, v29 offset:26624
	s_waitcnt vmcnt(5)
	v_mul_f32_e32 v8, 0xbfb8aa3b, v30
	v_exp_f32_e32 v8, v8
	s_nop 0
	v_add_f32_e32 v8, 1.0, v8
	v_div_scale_f32 v9, s[10:11], v8, v8, 1.0
	v_rcp_f32_e32 v10, v9
	v_div_scale_f32 v11, vcc, 1.0, v8, 1.0
	v_fma_f32 v12, -v9, v10, 1.0
	v_fmac_f32_e32 v10, v12, v10
	v_mul_f32_e32 v12, v11, v10
	v_fma_f32 v13, -v9, v12, v11
	v_fmac_f32_e32 v12, v13, v10
	v_fma_f32 v9, -v9, v12, v11
	v_div_fmas_f32 v9, v9, v10, v12
	v_div_fixup_f32 v8, v9, v8, 1.0
	v_mul_f32_e32 v30, v30, v8
	ds_write_b32 v6, v30 offset:28672
	s_waitcnt vmcnt(4)
	v_mul_f32_e32 v8, 0xbfb8aa3b, v31
	v_exp_f32_e32 v8, v8
	s_nop 0
	v_add_f32_e32 v8, 1.0, v8
	v_div_scale_f32 v9, s[10:11], v8, v8, 1.0
	v_rcp_f32_e32 v10, v9
	v_div_scale_f32 v11, vcc, 1.0, v8, 1.0
	v_fma_f32 v12, -v9, v10, 1.0
	v_fmac_f32_e32 v10, v12, v10
	v_mul_f32_e32 v12, v11, v10
	v_fma_f32 v13, -v9, v12, v11
	v_fmac_f32_e32 v12, v13, v10
	v_fma_f32 v9, -v9, v12, v11
	v_div_fmas_f32 v9, v9, v10, v12
	v_div_fixup_f32 v8, v9, v8, 1.0
	v_mul_f32_e32 v31, v31, v8
	ds_write_b32 v6, v31 offset:30720
	s_waitcnt vmcnt(3)
	v_mul_f32_e32 v8, 0xbfb8aa3b, v32
	v_exp_f32_e32 v8, v8
	s_nop 0
	v_add_f32_e32 v8, 1.0, v8
	v_div_scale_f32 v9, s[10:11], v8, v8, 1.0
	v_rcp_f32_e32 v10, v9
	v_div_scale_f32 v11, vcc, 1.0, v8, 1.0
	v_fma_f32 v12, -v9, v10, 1.0
	v_fmac_f32_e32 v10, v12, v10
	v_mul_f32_e32 v12, v11, v10
	v_fma_f32 v13, -v9, v12, v11
	v_fmac_f32_e32 v12, v13, v10
	v_fma_f32 v9, -v9, v12, v11
	v_div_fmas_f32 v9, v9, v10, v12
	v_div_fixup_f32 v8, v9, v8, 1.0
	v_mul_f32_e32 v32, v32, v8
	ds_write_b32 v6, v32 offset:32768
	s_waitcnt vmcnt(2)
	v_mul_f32_e32 v8, 0xbfb8aa3b, v33
	v_exp_f32_e32 v8, v8
	s_nop 0
	v_add_f32_e32 v8, 1.0, v8
	v_div_scale_f32 v9, s[10:11], v8, v8, 1.0
	v_rcp_f32_e32 v10, v9
	v_div_scale_f32 v11, vcc, 1.0, v8, 1.0
	v_fma_f32 v12, -v9, v10, 1.0
	v_fmac_f32_e32 v10, v12, v10
	v_mul_f32_e32 v12, v11, v10
	v_fma_f32 v13, -v9, v12, v11
	v_fmac_f32_e32 v12, v13, v10
	v_fma_f32 v9, -v9, v12, v11
	v_div_fmas_f32 v9, v9, v10, v12
	v_div_fixup_f32 v8, v9, v8, 1.0
	v_mul_f32_e32 v33, v33, v8
	ds_write_b32 v6, v33 offset:34816
	s_waitcnt vmcnt(1)
	v_mul_f32_e32 v8, 0xbfb8aa3b, v34
	v_exp_f32_e32 v8, v8
	s_nop 0
	v_add_f32_e32 v8, 1.0, v8
	v_div_scale_f32 v9, s[10:11], v8, v8, 1.0
	v_rcp_f32_e32 v10, v9
	v_div_scale_f32 v11, vcc, 1.0, v8, 1.0
	v_fma_f32 v12, -v9, v10, 1.0
	v_fmac_f32_e32 v10, v12, v10
	v_mul_f32_e32 v12, v11, v10
	v_fma_f32 v13, -v9, v12, v11
	v_fmac_f32_e32 v12, v13, v10
	v_fma_f32 v9, -v9, v12, v11
	v_div_fmas_f32 v9, v9, v10, v12
	v_div_fixup_f32 v8, v9, v8, 1.0
	v_mul_f32_e32 v34, v34, v8
	ds_write_b32 v6, v34 offset:36864
	s_waitcnt vmcnt(0)
	v_mul_f32_e32 v8, 0xbfb8aa3b, v35
	v_exp_f32_e32 v8, v8
	s_nop 0
	v_add_f32_e32 v8, 1.0, v8
	v_div_scale_f32 v9, s[10:11], v8, v8, 1.0
	v_rcp_f32_e32 v10, v9
	v_div_scale_f32 v11, vcc, 1.0, v8, 1.0
	v_fma_f32 v12, -v9, v10, 1.0
	v_fmac_f32_e32 v10, v12, v10
	v_mul_f32_e32 v12, v11, v10
	v_fma_f32 v13, -v9, v12, v11
	v_fmac_f32_e32 v12, v13, v10
	v_fma_f32 v9, -v9, v12, v11
	v_div_fmas_f32 v9, v9, v10, v12
	v_div_fixup_f32 v8, v9, v8, 1.0
	v_mul_f32_e32 v35, v35, v8
	ds_write_b32 v6, v35 offset:38912

; #define LAS __attribute__((address_space(3)))
; __device__ __forceinline__ float sigmoid_(float x) { return 1.f / (1.f + __expf(-x)); }
; __device__ __forceinline__ float silu_(float x) { return x * sigmoid_(x); }
; __device__ __forceinline__ void mod_items(const Args& a, const Ctx& c0, int l) {
;     ...
;     __syncthreads();
;     LAS float* sc = (LAS float*)c.lds;
;     LAS float* red = (LAS float*)(c.lds + 40960);
;     for (int i = c.tid; i < 5 * DM; i += 512) { const int r = i >> 11, k = i & 2047; const float v = r < 4 ? INP(1)[r * DM + k] : INP(3)[k]; sc[i] = silu_(v); }
;     __syncthreads();
.LBB0_1684:
	v_lshlrev_b32_e32 v3, 2, v2
	global_load_dword v16, v3, s[42:43]
	v_add_u32_e32 v3, 0x800, v3
	global_load_dword v17, v3, s[42:43]
	v_add_u32_e32 v3, 0x800, v3
	global_load_dword v18, v3, s[42:43]
	v_add_u32_e32 v3, 0x800, v3
	global_load_dword v19, v3, s[42:43]
	v_add_u32_e32 v3, 0x800, v3
	global_load_dword v20, v3, s[42:43]
	v_add_u32_e32 v3, 0x800, v3
	global_load_dword v21, v3, s[42:43]
	v_add_u32_e32 v3, 0x800, v3
	global_load_dword v22, v3, s[42:43]
	v_add_u32_e32 v3, 0x800, v3
	global_load_dword v23, v3, s[42:43]
	v_add_u32_e32 v3, 0x800, v3
	global_load_dword v24, v3, s[42:43]
	v_add_u32_e32 v3, 0x800, v3
	global_load_dword v25, v3, s[42:43]
	v_add_u32_e32 v3, 0x800, v3
	global_load_dword v26, v3, s[42:43]
	v_add_u32_e32 v3, 0x800, v3
	global_load_dword v27, v3, s[42:43]
	v_add_u32_e32 v3, 0x800, v3
	global_load_dword v28, v3, s[42:43]
	v_add_u32_e32 v3, 0x800, v3
	global_load_dword v29, v3, s[42:43]
	v_add_u32_e32 v3, 0x800, v3
	global_load_dword v30, v3, s[42:43]
	v_add_u32_e32 v3, 0x800, v3
	global_load_dword v31, v3, s[42:43]
	v_lshlrev_b32_e32 v3, 2, v2
	global_load_dword v32, v3, s[46:47]
	v_add_u32_e32 v3, 0x800, v3
	global_load_dword v33, v3, s[46:47]
	v_add_u32_e32 v3, 0x800, v3
	global_load_dword v34, v3, s[46:47]
	v_add_u32_e32 v3, 0x800, v3
	global_load_dword v35, v3, s[46:47]
	s_waitcnt vmcnt(19)
	v_mul_f32_e32 v7, 0xbfb8aa3b, v16
	v_exp_f32_e32 v7, v7
	s_nop 0
	v_add_f32_e32 v7, 1.0, v7
	v_div_scale_f32 v8, s[8:9], v7, v7, 1.0
	v_rcp_f32_e32 v9, v8
	v_div_scale_f32 v10, vcc, 1.0, v7, 1.0
	v_fma_f32 v11, -v8, v9, 1.0
	v_fmac_f32_e32 v9, v11, v9
	v_mul_f32_e32 v11, v10, v9
	v_fma_f32 v12, -v8, v11, v10
	v_fmac_f32_e32 v11, v12, v9
	v_fma_f32 v8, -v8, v11, v10
	v_div_fmas_f32 v8, v8, v9, v11
	v_div_fixup_f32 v7, v8, v7, 1.0
	v_mul_f32_e32 v16, v16, v7
	ds_write_b32 v6, v16
	s_waitcnt vmcnt(18)
	v_mul_f32_e32 v7, 0xbfb8aa3b, v17
	v_exp_f32_e32 v7, v7
	s_nop 0
	v_add_f32_e32 v7, 1.0, v7
	v_div_scale_f32 v8, s[8:9], v7, v7, 1.0
	v_rcp_f32_e32 v9, v8
	v_div_scale_f32 v10, vcc, 1.0, v7, 1.0
	v_fma_f32 v11, -v8, v9, 1.0
	v_fmac_f32_e32 v9, v11, v9
	v_mul_f32_e32 v11, v10, v9
	v_fma_f32 v12, -v8, v11, v10
	v_fmac_f32_e32 v11, v12, v9
	v_fma_f32 v8, -v8, v11, v10
	v_div_fmas_f32 v8, v8, v9, v11
	v_div_fixup_f32 v7, v8, v7, 1.0
	v_mul_f32_e32 v17, v17, v7
	ds_write_b32 v6, v17 offset:2048
	s_waitcnt vmcnt(17)
	v_mul_f32_e32 v7, 0xbfb8aa3b, v18
	v_exp_f32_e32 v7, v7
	s_nop 0
	v_add_f32_e32 v7, 1.0, v7
	v_div_scale_f32 v8, s[8:9], v7, v7, 1.0
	v_rcp_f32_e32 v9, v8
	v_div_scale_f32 v10, vcc, 1.0, v7, 1.0
	v_fma_f32 v11, -v8, v9, 1.0
	v_fmac_f32_e32 v9, v11, v9
	v_mul_f32_e32 v11, v10, v9
	v_fma_f32 v12, -v8, v11, v10
	v_fmac_f32_e32 v11, v12, v9
	v_fma_f32 v8, -v8, v11, v10
	v_div_fmas_f32 v8, v8, v9, v11
	v_div_fixup_f32 v7, v8, v7, 1.0
	v_mul_f32_e32 v18, v18, v7
	ds_write_b32 v6, v18 offset:4096
	s_waitcnt vmcnt(16)
	v_mul_f32_e32 v7, 0xbfb8aa3b, v19
	v_exp_f32_e32 v7, v7
	s_nop 0
	v_add_f32_e32 v7, 1.0, v7
	v_div_scale_f32 v8, s[8:9], v7, v7, 1.0
	v_rcp_f32_e32 v9, v8
	v_div_scale_f32 v10, vcc, 1.0, v7, 1.0
	v_fma_f32 v11, -v8, v9, 1.0
	v_fmac_f32_e32 v9, v11, v9
	v_mul_f32_e32 v11, v10, v9
	v_fma_f32 v12, -v8, v11, v10
	v_fmac_f32_e32 v11, v12, v9
	v_fma_f32 v8, -v8, v11, v10
	v_div_fmas_f32 v8, v8, v9, v11
	v_div_fixup_f32 v7, v8, v7, 1.0
	v_mul_f32_e32 v19, v19, v7
	ds_write_b32 v6, v19 offset:6144
	s_waitcnt vmcnt(15)
	v_mul_f32_e32 v7, 0xbfb8aa3b, v20
	v_exp_f32_e32 v7, v7
	s_nop 0
	v_add_f32_e32 v7, 1.0, v7
	v_div_scale_f32 v8, s[8:9], v7, v7, 1.0
	v_rcp_f32_e32 v9, v8
	v_div_scale_f32 v10, vcc, 1.0, v7, 1.0
	v_fma_f32 v11, -v8, v9, 1.0
	v_fmac_f32_e32 v9, v11, v9
	v_mul_f32_e32 v11, v10, v9
	v_fma_f32 v12, -v8, v11, v10
	v_fmac_f32_e32 v11, v12, v9
	v_fma_f32 v8, -v8, v11, v10
	v_div_fmas_f32 v8, v8, v9, v11
	v_div_fixup_f32 v7, v8, v7, 1.0
	v_mul_f32_e32 v20, v20, v7
	ds_write_b32 v6, v20 offset:8192
	s_waitcnt vmcnt(14)
	v_mul_f32_e32 v7, 0xbfb8aa3b, v21
	v_exp_f32_e32 v7, v7
	s_nop 0
	v_add_f32_e32 v7, 1.0, v7
	v_div_scale_f32 v8, s[8:9], v7, v7, 1.0
	v_rcp_f32_e32 v9, v8
	v_div_scale_f32 v10, vcc, 1.0, v7, 1.0
	v_fma_f32 v11, -v8, v9, 1.0
	v_fmac_f32_e32 v9, v11, v9
	v_mul_f32_e32 v11, v10, v9
	v_fma_f32 v12, -v8, v11, v10
	v_fmac_f32_e32 v11, v12, v9
	v_fma_f32 v8, -v8, v11, v10
	v_div_fmas_f32 v8, v8, v9, v11
	v_div_fixup_f32 v7, v8, v7, 1.0
	v_mul_f32_e32 v21, v21, v7
	ds_write_b32 v6, v21 offset:10240
	s_waitcnt vmcnt(13)
	v_mul_f32_e32 v7, 0xbfb8aa3b, v22
	v_exp_f32_e32 v7, v7
	s_nop 0
	v_add_f32_e32 v7, 1.0, v7
	v_div_scale_f32 v8, s[8:9], v7, v7, 1.0
	v_rcp_f32_e32 v9, v8
	v_div_scale_f32 v10, vcc, 1.0, v7, 1.0
	v_fma_f32 v11, -v8, v9, 1.0
	v_fmac_f32_e32 v9, v11, v9
	v_mul_f32_e32 v11, v10, v9
	v_fma_f32 v12, -v8, v11, v10
	v_fmac_f32_e32 v11, v12, v9
	v_fma_f32 v8, -v8, v11, v10
	v_div_fmas_f32 v8, v8, v9, v11
	v_div_fixup_f32 v7, v8, v7, 1.0
	v_mul_f32_e32 v22, v22, v7
	ds_write_b32 v6, v22 offset:12288
	s_waitcnt vmcnt(12)
	v_mul_f32_e32 v7, 0xbfb8aa3b, v23
	v_exp_f32_e32 v7, v7
	s_nop 0
	v_add_f32_e32 v7, 1.0, v7
	v_div_scale_f32 v8, s[8:9], v7, v7, 1.0
	v_rcp_f32_e32 v9, v8
	v_div_scale_f32 v10, vcc, 1.0, v7, 1.0
	v_fma_f32 v11, -v8, v9, 1.0
	v_fmac_f32_e32 v9, v11, v9
	v_mul_f32_e32 v11, v10, v9
	v_fma_f32 v12, -v8, v11, v10
	v_fmac_f32_e32 v11, v12, v9
	v_fma_f32 v8, -v8, v11, v10
	v_div_fmas_f32 v8, v8, v9, v11
	v_div_fixup_f32 v7, v8, v7, 1.0
	v_mul_f32_e32 v23, v23, v7
	ds_write_b32 v6, v23 offset:14336
	s_waitcnt vmcnt(11)
; #define LAS __attribute__((address_space(3)))
; __device__ __forceinline__ float sigmoid_(float x) { return 1.f / (1.f + __expf(-x)); }
; __device__ __forceinline__ float silu_(float x) { return x * sigmoid_(x); }
; __device__ __forceinline__ void mod_items(const Args& a, const Ctx& c0, int l) {
;     ...
;     __syncthreads();
;     LAS float* sc = (LAS float*)c.lds;
;     LAS float* red = (LAS float*)(c.lds + 40960);
;     for (int i = c.tid; i < 5 * DM; i += 512) { const int r = i >> 11, k = i & 2047; const float v = r < 4 ? INP(1)[r * DM + k] : INP(3)[k]; sc[i] = silu_(v); }
;     __syncthreads();
	v_mul_f32_e32 v7, 0xbfb8aa3b, v24
	v_exp_f32_e32 v7, v7
	s_nop 0
	v_add_f32_e32 v7, 1.0, v7
	v_div_scale_f32 v8, s[8:9], v7, v7, 1.0
	v_rcp_f32_e32 v9, v8
	v_div_scale_f32 v10, vcc, 1.0, v7, 1.0
	v_fma_f32 v11, -v8, v9, 1.0
	v_fmac_f32_e32 v9, v11, v9
	v_mul_f32_e32 v11, v10, v9
	v_fma_f32 v12, -v8, v11, v10
	v_fmac_f32_e32 v11, v12, v9
	v_fma_f32 v8, -v8, v11, v10
	v_div_fmas_f32 v8, v8, v9, v11
	v_div_fixup_f32 v7, v8, v7, 1.0
	v_mul_f32_e32 v24, v24, v7
	ds_write_b32 v6, v24 offset:16384
	s_waitcnt vmcnt(10)
	v_mul_f32_e32 v7, 0xbfb8aa3b, v25
	v_exp_f32_e32 v7, v7
	s_nop 0
	v_add_f32_e32 v7, 1.0, v7
	v_div_scale_f32 v8, s[8:9], v7, v7, 1.0
	v_rcp_f32_e32 v9, v8
	v_div_scale_f32 v10, vcc, 1.0, v7, 1.0
	v_fma_f32 v11, -v8, v9, 1.0
	v_fmac_f32_e32 v9, v11, v9
	v_mul_f32_e32 v11, v10, v9
	v_fma_f32 v12, -v8, v11, v10
	v_fmac_f32_e32 v11, v12, v9
	v_fma_f32 v8, -v8, v11, v10
	v_div_fmas_f32 v8, v8, v9, v11
	v_div_fixup_f32 v7, v8, v7, 1.0
	v_mul_f32_e32 v25, v25, v7
	ds_write_b32 v6, v25 offset:18432
	s_waitcnt vmcnt(9)
	v_mul_f32_e32 v7, 0xbfb8aa3b, v26
	v_exp_f32_e32 v7, v7
	s_nop 0
	v_add_f32_e32 v7, 1.0, v7
	v_div_scale_f32 v8, s[8:9], v7, v7, 1.0
	v_rcp_f32_e32 v9, v8
	v_div_scale_f32 v10, vcc, 1.0, v7, 1.0
	v_fma_f32 v11, -v8, v9, 1.0
	v_fmac_f32_e32 v9, v11, v9
	v_mul_f32_e32 v11, v10, v9
	v_fma_f32 v12, -v8, v11, v10
	v_fmac_f32_e32 v11, v12, v9
	v_fma_f32 v8, -v8, v11, v10
	v_div_fmas_f32 v8, v8, v9, v11
	v_div_fixup_f32 v7, v8, v7, 1.0
	v_mul_f32_e32 v26, v26, v7
	ds_write_b32 v6, v26 offset:20480
	s_waitcnt vmcnt(8)
	v_mul_f32_e32 v7, 0xbfb8aa3b, v27
	v_exp_f32_e32 v7, v7
	s_nop 0
	v_add_f32_e32 v7, 1.0, v7
	v_div_scale_f32 v8, s[8:9], v7, v7, 1.0
	v_rcp_f32_e32 v9, v8
	v_div_scale_f32 v10, vcc, 1.0, v7, 1.0
	v_fma_f32 v11, -v8, v9, 1.0
	v_fmac_f32_e32 v9, v11, v9
	v_mul_f32_e32 v11, v10, v9
	v_fma_f32 v12, -v8, v11, v10
	v_fmac_f32_e32 v11, v12, v9
	v_fma_f32 v8, -v8, v11, v10
	v_div_fmas_f32 v8, v8, v9, v11
	v_div_fixup_f32 v7, v8, v7, 1.0
	v_mul_f32_e32 v27, v27, v7
	ds_write_b32 v6, v27 offset:22528
	s_waitcnt vmcnt(7)
	v_mul_f32_e32 v7, 0xbfb8aa3b, v28
	v_exp_f32_e32 v7, v7
	s_nop 0
	v_add_f32_e32 v7, 1.0, v7
	v_div_scale_f32 v8, s[8:9], v7, v7, 1.0
	v_rcp_f32_e32 v9, v8
	v_div_scale_f32 v10, vcc, 1.0, v7, 1.0
	v_fma_f32 v11, -v8, v9, 1.0
	v_fmac_f32_e32 v9, v11, v9
	v_mul_f32_e32 v11, v10, v9
	v_fma_f32 v12, -v8, v11, v10
	v_fmac_f32_e32 v11, v12, v9
	v_fma_f32 v8, -v8, v11, v10
	v_div_fmas_f32 v8, v8, v9, v11
	v_div_fixup_f32 v7, v8, v7, 1.0
	v_mul_f32_e32 v28, v28, v7
	ds_write_b32 v6, v28 offset:24576
	s_waitcnt vmcnt(6)
	v_mul_f32_e32 v7, 0xbfb8aa3b, v29
	v_exp_f32_e32 v7, v7
	s_nop 0
	v_add_f32_e32 v7, 1.0, v7
	v_div_scale_f32 v8, s[8:9], v7, v7, 1.0
	v_rcp_f32_e32 v9, v8
	v_div_scale_f32 v10, vcc, 1.0, v7, 1.0
	v_fma_f32 v11, -v8, v9, 1.0
	v_fmac_f32_e32 v9, v11, v9
	v_mul_f32_e32 v11, v10, v9
	v_fma_f32 v12, -v8, v11, v10
	v_fmac_f32_e32 v11, v12, v9
	v_fma_f32 v8, -v8, v11, v10
	v_div_fmas_f32 v8, v8, v9, v11
	v_div_fixup_f32 v7, v8, v7, 1.0
	v_mul_f32_e32 v29, v29, v7
	ds_write_b32 v6, v29 offset:26624
	s_waitcnt vmcnt(5)
	v_mul_f32_e32 v7, 0xbfb8aa3b, v30
	v_exp_f32_e32 v7, v7
	s_nop 0
	v_add_f32_e32 v7, 1.0, v7
	v_div_scale_f32 v8, s[8:9], v7, v7, 1.0
	v_rcp_f32_e32 v9, v8
	v_div_scale_f32 v10, vcc, 1.0, v7, 1.0
	v_fma_f32 v11, -v8, v9, 1.0
	v_fmac_f32_e32 v9, v11, v9
	v_mul_f32_e32 v11, v10, v9
	v_fma_f32 v12, -v8, v11, v10
	v_fmac_f32_e32 v11, v12, v9
	v_fma_f32 v8, -v8, v11, v10
	v_div_fmas_f32 v8, v8, v9, v11
	v_div_fixup_f32 v7, v8, v7, 1.0
	v_mul_f32_e32 v30, v30, v7
	ds_write_b32 v6, v30 offset:28672
	s_waitcnt vmcnt(4)
	v_mul_f32_e32 v7, 0xbfb8aa3b, v31
	v_exp_f32_e32 v7, v7
	s_nop 0
	v_add_f32_e32 v7, 1.0, v7
	v_div_scale_f32 v8, s[8:9], v7, v7, 1.0
	v_rcp_f32_e32 v9, v8
	v_div_scale_f32 v10, vcc, 1.0, v7, 1.0
	v_fma_f32 v11, -v8, v9, 1.0
	v_fmac_f32_e32 v9, v11, v9
	v_mul_f32_e32 v11, v10, v9
	v_fma_f32 v12, -v8, v11, v10
	v_fmac_f32_e32 v11, v12, v9
	v_fma_f32 v8, -v8, v11, v10
	v_div_fmas_f32 v8, v8, v9, v11
	v_div_fixup_f32 v7, v8, v7, 1.0
	v_mul_f32_e32 v31, v31, v7
	ds_write_b32 v6, v31 offset:30720
	s_waitcnt vmcnt(3)
	v_mul_f32_e32 v7, 0xbfb8aa3b, v32
	v_exp_f32_e32 v7, v7
	s_nop 0
	v_add_f32_e32 v7, 1.0, v7
	v_div_scale_f32 v8, s[8:9], v7, v7, 1.0
	v_rcp_f32_e32 v9, v8
	v_div_scale_f32 v10, vcc, 1.0, v7, 1.0
	v_fma_f32 v11, -v8, v9, 1.0
	v_fmac_f32_e32 v9, v11, v9
	v_mul_f32_e32 v11, v10, v9
	v_fma_f32 v12, -v8, v11, v10
	v_fmac_f32_e32 v11, v12, v9
	v_fma_f32 v8, -v8, v11, v10
	v_div_fmas_f32 v8, v8, v9, v11
	v_div_fixup_f32 v7, v8, v7, 1.0
	v_mul_f32_e32 v32, v32, v7
	ds_write_b32 v6, v32 offset:32768
	s_waitcnt vmcnt(2)
	v_mul_f32_e32 v7, 0xbfb8aa3b, v33
	v_exp_f32_e32 v7, v7
	s_nop 0
	v_add_f32_e32 v7, 1.0, v7
	v_div_scale_f32 v8, s[8:9], v7, v7, 1.0
	v_rcp_f32_e32 v9, v8
	v_div_scale_f32 v10, vcc, 1.0, v7, 1.0
	v_fma_f32 v11, -v8, v9, 1.0
	v_fmac_f32_e32 v9, v11, v9
	v_mul_f32_e32 v11, v10, v9
	v_fma_f32 v12, -v8, v11, v10
	v_fmac_f32_e32 v11, v12, v9
	v_fma_f32 v8, -v8, v11, v10
	v_div_fmas_f32 v8, v8, v9, v11
	v_div_fixup_f32 v7, v8, v7, 1.0
	v_mul_f32_e32 v33, v33, v7
	ds_write_b32 v6, v33 offset:34816
	s_waitcnt vmcnt(1)
	v_mul_f32_e32 v7, 0xbfb8aa3b, v34
	v_exp_f32_e32 v7, v7
	s_nop 0
	v_add_f32_e32 v7, 1.0, v7
	v_div_scale_f32 v8, s[8:9], v7, v7, 1.0
	v_rcp_f32_e32 v9, v8
	v_div_scale_f32 v10, vcc, 1.0, v7, 1.0
	v_fma_f32 v11, -v8, v9, 1.0
	v_fmac_f32_e32 v9, v11, v9
	v_mul_f32_e32 v11, v10, v9
	v_fma_f32 v12, -v8, v11, v10
	v_fmac_f32_e32 v11, v12, v9
	v_fma_f32 v8, -v8, v11, v10
	v_div_fmas_f32 v8, v8, v9, v11
	v_div_fixup_f32 v7, v8, v7, 1.0
	v_mul_f32_e32 v34, v34, v7
	ds_write_b32 v6, v34 offset:36864
	s_waitcnt vmcnt(0)
	v_mul_f32_e32 v7, 0xbfb8aa3b, v35
	v_exp_f32_e32 v7, v7
	s_nop 0
	v_add_f32_e32 v7, 1.0, v7
	v_div_scale_f32 v8, s[8:9], v7, v7, 1.0
	v_rcp_f32_e32 v9, v8
	v_div_scale_f32 v10, vcc, 1.0, v7, 1.0
	v_fma_f32 v11, -v8, v9, 1.0
	v_fmac_f32_e32 v9, v11, v9
	v_mul_f32_e32 v11, v10, v9
	v_fma_f32 v12, -v8, v11, v10
	v_fmac_f32_e32 v11, v12, v9
	v_fma_f32 v8, -v8, v11, v10
	v_div_fmas_f32 v8, v8, v9, v11
	v_div_fixup_f32 v7, v8, v7, 1.0
	v_mul_f32_e32 v35, v35, v7
	ds_write_b32 v6, v35 offset:38912
